# out-projection GEMM gated-residual epilogue de-serialised: 12 residual loads in flight with counted vmcnt instead of one load per vmcnt(0); plus MLA key-loop reorder
# speedup vs baseline: 1.0022x; 1.0022x over previous
; #define xl OUTP(launder(kargs))
;     __device__ __forceinline__ void operator()(const f32x4 (&acc)[2][2][4][2], const Unit& u, int wr, int wc, int fr, int fq) const {
;         const int b = u.pm / 33, j = u.pm - b * 33;
;         float* base = (j < 32) ? xl + ((size_t)(b * SEQ + j * 256)) * DM : xc + ((size_t)(b * CTXL)) * DM;
;         const float* gv = mod + ((j < 32 ? b : 8) * 6 + gk) * 1024;
;         const int rl0 = wr * 64 + fr; const int col0 = u.pn * BM + wc * 32 + 4 * fq;
;         f32x4 g[2][2];
; #pragma unroll
;         for (int bj = 0; bj < 2; ++bj)
; #pragma unroll
;             for (int n = 0; n < 2; ++n) g[bj][n] = *(const f32x4*)(gv + col0 + bj * HALF + n * 16);
; #pragma unroll
;         for (int ai = 0; ai < 2; ++ai)
; #pragma unroll
;             for (int m = 0; m < 4; ++m) { float* rowp = base + (size_t)(rl0 + ai * HALF + m * 16) * DM + col0;
; #pragma unroll
;                 for (int bj = 0; bj < 2; ++bj)
; #pragma unroll
;                     for (int n = 0; n < 2; ++n) { f32x4* p = (f32x4*)(rowp + bj * HALF + n * 16); const f32x4 xv = *p; *p = xv + g[bj][n] * acc[ai][bj][m][n]; }
;                 asm volatile("" ::: "memory"); }
.LBB0_1130:
	s_lshl_b64 s[22:23], s[22:23], 2
	v_lshl_or_b32 v90, s59, 8, v171
	s_add_u32 s22, s49, s22
	v_ashrrev_i32_e32 v91, 31, v90
	s_addc_u32 s23, s50, s23
	v_lshlrev_b64 v[168:169], 2, v[90:91]
	v_lshl_add_u64 v[90:91], s[22:23], 0, v[168:169]
	v_lshl_add_u64 v[168:169], s[14:15], 0, v[168:169]
	global_load_dwordx4 v[110:113], v[90:91], off
	global_load_dwordx4 v[102:105], v[90:91], off offset:64
	global_load_dwordx4 v[98:101], v[90:91], off offset:512
	s_nop 0
	global_load_dwordx4 v[90:93], v[90:91], off offset:576
	s_mov_b64 s[14:15], -1
	s_andn2_b64 vcc, exec, s[4:5]
	v_lshl_add_u64 v[222:223], v[168:169], 0, v[148:149]
	global_load_dwordx4 v[174:177], v[222:223], off
	global_load_dwordx4 v[178:181], v[222:223], off offset:64
	global_load_dwordx4 v[182:185], v[222:223], off offset:512
	global_load_dwordx4 v[186:189], v[222:223], off offset:576
	v_lshl_add_u64 v[236:237], v[168:169], 0, v[150:151]
	global_load_dwordx4 v[190:193], v[236:237], off
	global_load_dwordx4 v[198:201], v[236:237], off offset:64
	global_load_dwordx4 v[202:205], v[236:237], off offset:512
	global_load_dwordx4 v[206:209], v[236:237], off offset:576
	v_lshl_add_u64 v[238:239], v[168:169], 0, v[152:153]
	global_load_dwordx4 v[210:213], v[238:239], off
	global_load_dwordx4 v[214:217], v[238:239], off offset:64
	global_load_dwordx4 v[218:221], v[238:239], off offset:512
	global_load_dwordx4 v[228:231], v[238:239], off offset:576
	s_waitcnt vmcnt(8)
	v_pk_fma_f32 v[144:145], v[144:145], v[112:113], v[176:177]
	v_pk_fma_f32 v[142:143], v[142:143], v[110:111], v[174:175]
	v_pk_fma_f32 v[140:141], v[140:141], v[104:105], v[180:181]
	v_pk_fma_f32 v[138:139], v[138:139], v[102:103], v[178:179]
	v_pk_fma_f32 v[136:137], v[136:137], v[100:101], v[184:185]
	v_pk_fma_f32 v[134:135], v[134:135], v[98:99], v[182:183]
	v_pk_fma_f32 v[132:133], v[132:133], v[92:93], v[188:189]
	v_pk_fma_f32 v[130:131], v[130:131], v[90:91], v[186:187]
	global_store_dwordx4 v[222:223], v[142:145], off
	global_store_dwordx4 v[222:223], v[138:141], off offset:64
	global_store_dwordx4 v[222:223], v[134:137], off offset:512
	global_store_dwordx4 v[222:223], v[130:133], off offset:576
	v_lshl_add_u64 v[240:241], v[168:169], 0, v[154:155]
	global_load_dwordx4 v[142:145], v[240:241], off
	global_load_dwordx4 v[138:141], v[240:241], off offset:64
	global_load_dwordx4 v[134:137], v[240:241], off offset:512
	global_load_dwordx4 v[130:133], v[240:241], off offset:576
	s_waitcnt vmcnt(12)
	v_pk_fma_f32 v[128:129], v[128:129], v[112:113], v[192:193]
	v_pk_fma_f32 v[126:127], v[126:127], v[110:111], v[190:191]
	v_pk_fma_f32 v[124:125], v[124:125], v[104:105], v[200:201]
	v_pk_fma_f32 v[122:123], v[122:123], v[102:103], v[198:199]
	v_pk_fma_f32 v[120:121], v[120:121], v[100:101], v[204:205]
	v_pk_fma_f32 v[118:119], v[118:119], v[98:99], v[202:203]
	v_pk_fma_f32 v[116:117], v[116:117], v[92:93], v[208:209]
	v_pk_fma_f32 v[114:115], v[114:115], v[90:91], v[206:207]
	global_store_dwordx4 v[236:237], v[126:129], off
	global_store_dwordx4 v[236:237], v[122:125], off offset:64
	global_store_dwordx4 v[236:237], v[118:121], off offset:512
	global_store_dwordx4 v[236:237], v[114:117], off offset:576
	v_lshl_add_u64 v[222:223], v[168:169], 0, v[156:157]
	global_load_dwordx4 v[126:129], v[222:223], off
	global_load_dwordx4 v[122:125], v[222:223], off offset:64
	global_load_dwordx4 v[118:121], v[222:223], off offset:512
	global_load_dwordx4 v[114:117], v[222:223], off offset:576
	s_waitcnt vmcnt(16)
	v_pk_fma_f32 v[108:109], v[108:109], v[112:113], v[212:213]
	v_pk_fma_f32 v[106:107], v[106:107], v[110:111], v[210:211]
	v_pk_fma_f32 v[96:97], v[96:97], v[104:105], v[216:217]
	v_pk_fma_f32 v[94:95], v[94:95], v[102:103], v[214:215]
	v_pk_fma_f32 v[88:89], v[88:89], v[100:101], v[220:221]
	v_pk_fma_f32 v[86:87], v[86:87], v[98:99], v[218:219]
	v_pk_fma_f32 v[84:85], v[84:85], v[92:93], v[230:231]
	v_pk_fma_f32 v[82:83], v[82:83], v[90:91], v[228:229]
	global_store_dwordx4 v[238:239], v[106:109], off
	global_store_dwordx4 v[238:239], v[94:97], off offset:64
	global_store_dwordx4 v[238:239], v[86:89], off offset:512
	global_store_dwordx4 v[238:239], v[82:85], off offset:576
	v_lshl_add_u64 v[236:237], v[168:169], 0, v[158:159]
	global_load_dwordx4 v[106:109], v[236:237], off
	global_load_dwordx4 v[94:97], v[236:237], off offset:64
	global_load_dwordx4 v[86:89], v[236:237], off offset:512
	global_load_dwordx4 v[82:85], v[236:237], off offset:576
	s_waitcnt vmcnt(16)
;     __device__ __forceinline__ void operator()(const f32x4 (&acc)[2][2][4][2], const Unit& u, int wr, int wc, int fr, int fq) const {
;     ...
;             for (int m = 0; m < 4; ++m) { float* rowp = base + (size_t)(rl0 + ai * HALF + m * 16) * DM + col0;
; #pragma unroll
;                 for (int bj = 0; bj < 2; ++bj)
; #pragma unroll
;                     for (int n = 0; n < 2; ++n) { f32x4* p = (f32x4*)(rowp + bj * HALF + n * 16); const f32x4 xv = *p; *p = xv + g[bj][n] * acc[ai][bj][m][n]; }
;                 asm volatile("" ::: "memory"); }
	v_pk_fma_f32 v[80:81], v[80:81], v[112:113], v[144:145]
	v_pk_fma_f32 v[78:79], v[78:79], v[110:111], v[142:143]
	v_pk_fma_f32 v[76:77], v[76:77], v[104:105], v[140:141]
	v_pk_fma_f32 v[74:75], v[74:75], v[102:103], v[138:139]
	v_pk_fma_f32 v[72:73], v[72:73], v[100:101], v[136:137]
	v_pk_fma_f32 v[70:71], v[70:71], v[98:99], v[134:135]
	v_pk_fma_f32 v[68:69], v[68:69], v[92:93], v[132:133]
	v_pk_fma_f32 v[66:67], v[66:67], v[90:91], v[130:131]
	global_store_dwordx4 v[240:241], v[78:81], off
	global_store_dwordx4 v[240:241], v[74:77], off offset:64
	global_store_dwordx4 v[240:241], v[70:73], off offset:512
	global_store_dwordx4 v[240:241], v[66:69], off offset:576
	v_lshl_add_u64 v[238:239], v[168:169], 0, v[160:161]
	global_load_dwordx4 v[78:81], v[238:239], off
	global_load_dwordx4 v[74:77], v[238:239], off offset:64
	global_load_dwordx4 v[70:73], v[238:239], off offset:512
	global_load_dwordx4 v[66:69], v[238:239], off offset:576
	s_waitcnt vmcnt(16)
	v_pk_fma_f32 v[64:65], v[64:65], v[112:113], v[128:129]
	v_pk_fma_f32 v[62:63], v[62:63], v[110:111], v[126:127]
	v_pk_fma_f32 v[60:61], v[60:61], v[104:105], v[124:125]
	v_pk_fma_f32 v[58:59], v[58:59], v[102:103], v[122:123]
	v_pk_fma_f32 v[56:57], v[56:57], v[100:101], v[120:121]
	v_pk_fma_f32 v[54:55], v[54:55], v[98:99], v[118:119]
	v_pk_fma_f32 v[52:53], v[52:53], v[92:93], v[116:117]
	v_pk_fma_f32 v[50:51], v[50:51], v[90:91], v[114:115]
	global_store_dwordx4 v[222:223], v[62:65], off
	global_store_dwordx4 v[222:223], v[58:61], off offset:64
	global_store_dwordx4 v[222:223], v[54:57], off offset:512
	global_store_dwordx4 v[222:223], v[50:53], off offset:576
	v_lshl_add_u64 v[240:241], v[168:169], 0, v[162:163]
	global_load_dwordx4 v[62:65], v[240:241], off
	global_load_dwordx4 v[58:61], v[240:241], off offset:64
	global_load_dwordx4 v[54:57], v[240:241], off offset:512
	global_load_dwordx4 v[50:53], v[240:241], off offset:576
	s_waitcnt vmcnt(16)
	v_pk_fma_f32 v[48:49], v[48:49], v[112:113], v[108:109]
	v_pk_fma_f32 v[46:47], v[46:47], v[110:111], v[106:107]
	v_pk_fma_f32 v[44:45], v[44:45], v[104:105], v[96:97]
	v_pk_fma_f32 v[42:43], v[42:43], v[102:103], v[94:95]
	v_pk_fma_f32 v[40:41], v[40:41], v[100:101], v[88:89]
	v_pk_fma_f32 v[38:39], v[38:39], v[98:99], v[86:87]
	v_pk_fma_f32 v[36:37], v[36:37], v[92:93], v[84:85]
	v_pk_fma_f32 v[34:35], v[34:35], v[90:91], v[82:83]
	global_store_dwordx4 v[236:237], v[46:49], off
	global_store_dwordx4 v[236:237], v[42:45], off offset:64
	global_store_dwordx4 v[236:237], v[38:41], off offset:512
	global_store_dwordx4 v[236:237], v[34:37], off offset:576
	s_waitcnt vmcnt(12)
	v_pk_fma_f32 v[32:33], v[32:33], v[112:113], v[80:81]
	v_pk_fma_f32 v[30:31], v[30:31], v[110:111], v[78:79]
	v_pk_fma_f32 v[28:29], v[28:29], v[104:105], v[76:77]
	v_pk_fma_f32 v[26:27], v[26:27], v[102:103], v[74:75]
	v_pk_fma_f32 v[24:25], v[24:25], v[100:101], v[72:73]
	v_pk_fma_f32 v[22:23], v[22:23], v[98:99], v[70:71]
	v_pk_fma_f32 v[20:21], v[20:21], v[92:93], v[68:69]
	v_pk_fma_f32 v[18:19], v[18:19], v[90:91], v[66:67]
	global_store_dwordx4 v[238:239], v[30:33], off
	global_store_dwordx4 v[238:239], v[26:29], off offset:64
	global_store_dwordx4 v[238:239], v[22:25], off offset:512
	global_store_dwordx4 v[238:239], v[18:21], off offset:576
	s_waitcnt vmcnt(8)
	v_pk_fma_f32 v[16:17], v[16:17], v[112:113], v[64:65]
	v_pk_fma_f32 v[14:15], v[14:15], v[110:111], v[62:63]
	v_pk_fma_f32 v[12:13], v[12:13], v[104:105], v[60:61]
	v_pk_fma_f32 v[10:11], v[10:11], v[102:103], v[58:59]
	v_pk_fma_f32 v[8:9], v[8:9], v[100:101], v[56:57]
	v_pk_fma_f32 v[6:7], v[6:7], v[98:99], v[54:55]
	v_pk_fma_f32 v[4:5], v[4:5], v[92:93], v[52:53]
	v_pk_fma_f32 v[2:3], v[2:3], v[90:91], v[50:51]
	global_store_dwordx4 v[240:241], v[14:17], off
	global_store_dwordx4 v[240:241], v[10:13], off offset:64
	global_store_dwordx4 v[240:241], v[6:9], off offset:512
	global_store_dwordx4 v[240:241], v[2:5], off offset:576
	s_cbranch_vccnz .LBB0_1119
	s_andn2_b64 vcc, exec, s[8:9]
	s_cbranch_vccnz .LBB0_1118
	s_barrier
	s_branch .LBB0_1118
